# P5: p tile converted to bf16 once in GEMM prologue (stored to per-WG scratch), loop reads bf16 copy instead of f32 load+wait+cvt; plus static prio
# speedup vs baseline: 1.0074x; 1.0074x over previous
.LBB0_1548:
	s_lshl_b32 s40, s56, 7
	v_mov_b32_e32 v92, v0
	s_waitcnt vmcnt(0)
	s_waitcnt lgkmcnt(0)
	s_barrier
	s_ashr_i32 s41, s40, 31
	s_lshl_b64 s[0:1], s[40:41], 10
	v_ashrrev_i32_e32 v84, 4, v92
	v_add_u32_e32 v86, 32, v84
	v_add_u32_e32 v88, 64, v84
	s_add_u32 s0, s53, s0
	v_lshlrev_b32_e32 v4, 3, v92
	v_ashrrev_i32_e32 v85, 31, v84
	v_ashrrev_i32_e32 v87, 31, v86
	v_ashrrev_i32_e32 v89, 31, v88
	s_addc_u32 s1, s54, s1
	v_and_b32_e32 v165, 0x78, v4
	v_lshlrev_b64 v[4:5], 10, v[84:85]
	v_lshlrev_b64 v[12:13], 10, v[86:87]
	v_lshlrev_b64 v[20:21], 10, v[88:89]
	v_lshl_add_u64 v[168:169], s[0:1], 0, v[4:5]
	v_lshlrev_b32_e32 v28, 2, v165
	v_mov_b32_e32 v29, v2
	v_lshl_add_u64 v[170:171], s[0:1], 0, v[12:13]
	v_lshl_add_u64 v[172:173], s[0:1], 0, v[20:21]
	v_lshl_add_u64 v[40:41], v[168:169], 0, v[28:29]
	v_lshl_add_u64 v[48:49], v[170:171], 0, v[28:29]
	v_lshl_add_u64 v[56:57], v[172:173], 0, v[28:29]
	global_load_dwordx4 v[4:7], v[40:41], off offset:16
	global_load_dwordx4 v[8:11], v[40:41], off
	global_load_dwordx4 v[12:15], v[48:49], off offset:16
	global_load_dwordx4 v[16:19], v[48:49], off
	global_load_dwordx4 v[20:23], v[56:57], off offset:16
	global_load_dwordx4 v[24:27], v[56:57], off
	v_add_u32_e32 v90, 0x60, v84
	v_ashrrev_i32_e32 v91, 31, v90
	v_lshlrev_b64 v[30:31], 10, v[90:91]
	v_lshl_add_u64 v[174:175], s[0:1], 0, v[30:31]
	v_lshl_add_u64 v[64:65], v[174:175], 0, v[28:29]
	v_readlane_b32 s0, v251, 59
	v_readlane_b32 s1, v251, 60
	v_lshlrev_b32_e32 v168, 9, v84
	v_mov_b32_e32 v169, v2
	v_lshlrev_b32_e32 v244, 1, v165
	v_mov_b32_e32 v245, v2
	v_lshl_add_u64 v[168:169], s[0:1], 0, v[168:169]
	s_mov_b64 s[0:1], 0x4000
	v_lshl_add_u64 v[170:171], v[168:169], 0, s[0:1]
	s_mov_b64 s[0:1], 0x8000
	v_lshl_add_u64 v[172:173], v[168:169], 0, s[0:1]
	s_mov_b64 s[0:1], 0xc000
	v_lshl_add_u64 v[174:175], v[168:169], 0, s[0:1]
	v_lshl_add_u64 v[236:237], v[168:169], 0, v[244:245]
	v_lshl_add_u64 v[238:239], v[170:171], 0, v[244:245]
	v_lshl_add_u64 v[240:241], v[172:173], 0, v[244:245]
	v_lshl_add_u64 v[242:243], v[174:175], 0, v[244:245]
	global_load_dwordx4 v[28:31], v[64:65], off
	global_load_dwordx4 v[32:35], v[64:65], off offset:16
	global_load_dwordx4 v[36:39], v[40:41], off offset:512
	s_nop 0
	global_load_dwordx4 v[40:43], v[40:41], off offset:528
	s_nop 0
	global_load_dwordx4 v[44:47], v[48:49], off offset:512
	s_nop 0
	global_load_dwordx4 v[48:51], v[48:49], off offset:528
	s_nop 0
	global_load_dwordx4 v[52:55], v[56:57], off offset:512
	s_nop 0
	global_load_dwordx4 v[56:59], v[56:57], off offset:528
	s_nop 0
	global_load_dwordx4 v[60:63], v[64:65], off offset:512
	s_nop 0
	global_load_dwordx4 v[64:67], v[64:65], off offset:528
	s_lshl_b64 s[0:1], s[40:41], 11
	v_readfirstlane_b32 s12, v92
	s_add_u32 s0, s8, s0
	s_addc_u32 s1, s9, s1
	s_ashr_i32 s12, s12, 6
	s_cmp_lt_i32 s12, 8
	s_cselect_b64 s[38:39], -1, 0
	s_and_b64 s[42:43], s[38:39], exec
	s_cselect_b32 s41, s12, 7
	s_mul_hi_i32 s43, s41, 0x14000
	s_mul_i32 s41, s41, 0x14000
	v_and_b32_e32 v68, 63, v92
	s_add_u32 s42, s20, s41
	v_readlane_b32 s18, v248, 29
	v_mov_b32_e32 v69, v2
	v_lshlrev_b32_e32 v68, 4, v68
	s_addc_u32 s43, s52, s43
	v_readlane_b32 s19, v248, 30
	v_xor_b32_e32 v71, v84, v92
	v_lshl_add_u64 v[176:177], s[42:43], 0, v[68:69]
	s_mov_b32 s19, s21
	v_lshlrev_b32_e32 v70, 8, v84
	v_lshlrev_b32_e32 v71, 4, v71
	v_and_or_b32 v93, v71, s84, v70
	v_bfe_u32 v192, v92, 4, 2
	v_and_b32_e32 v167, 15, v92
	v_add_u32_e32 v193, 0, v93
	s_lshl_b32 s42, s12, 13
	s_lshl_b32 s41, s12, 5
	s_lshl_b32 s12, s12, 9
	s_mov_b32 s26, s18
	s_add_i32 s48, s42, 0
	s_add_i32 s49, s12, 0
	s_mov_b32 s60, 2
	s_mov_b32 s58, 1
	v_writelane_b32 v248, s26, 29
	s_mov_b32 s59, 0
	s_ashr_i32 s47, s41, 31
	s_add_i32 s48, s48, 0x10000
	s_add_i32 s49, s49, 0x20000
	s_mov_b32 s50, -2
	s_mov_b32 s51, 0
	s_mov_b32 s42, 0
	v_writelane_b32 v248, s27, 30
	s_waitcnt vmcnt(9)
	v_cvt_pk_bf16_f32 v80, v28, v29
	s_waitcnt vmcnt(8)
	v_cvt_pk_bf16_f32 v82, v32, v33
	v_lshl_add_u64 v[32:33], v[176:177], 0, s[18:19]
	v_cvt_pk_bf16_f32 v71, v6, v7
	v_cvt_pk_bf16_f32 v76, v24, v25
	v_cvt_pk_bf16_f32 v77, v26, v27
	v_cvt_pk_bf16_f32 v78, v20, v21
	v_cvt_pk_bf16_f32 v79, v22, v23
	v_cvt_pk_bf16_f32 v81, v30, v31
	s_waitcnt vmcnt(6)
	v_cvt_pk_bf16_f32 v6, v40, v41
	v_cvt_pk_bf16_f32 v7, v42, v43
	global_load_dwordx4 v[40:43], v[32:33], off
	global_load_dwordx4 v[28:31], v[32:33], off offset:1024
	global_load_dwordx4 v[24:27], v[32:33], off offset:2048
	global_load_dwordx4 v[20:23], v[32:33], off offset:3072
	v_add_co_u32_e32 v32, vcc, s22, v32
	v_cvt_pk_bf16_f32 v68, v8, v9
	s_nop 0
	v_addc_co_u32_e32 v33, vcc, 0, v33, vcc
	v_cvt_pk_bf16_f32 v69, v10, v11
	v_cvt_pk_bf16_f32 v70, v4, v5
	v_cvt_pk_bf16_f32 v74, v12, v13
	v_cvt_pk_bf16_f32 v4, v36, v37
	v_cvt_pk_bf16_f32 v5, v38, v39
	s_waitcnt vmcnt(9)
	v_cvt_pk_bf16_f32 v8, v44, v45
	v_cvt_pk_bf16_f32 v9, v46, v47
	s_waitcnt vmcnt(8)
	v_cvt_pk_bf16_f32 v10, v48, v49
	v_cvt_pk_bf16_f32 v11, v50, v51
	s_waitcnt vmcnt(7)
	v_cvt_pk_bf16_f32 v12, v52, v53
	v_cvt_pk_bf16_f32 v13, v54, v55
	global_load_dwordx4 v[52:55], v[32:33], off
	global_load_dwordx4 v[48:51], v[32:33], off offset:1024
	global_load_dwordx4 v[44:47], v[32:33], off offset:2048
	global_load_dwordx4 v[36:39], v[32:33], off offset:3072
	v_bitop3_b32 v32, v192, v92, 15 bitop3:0x78
	v_cvt_pk_bf16_f32 v83, v34, v35
	v_lshlrev_b32_e32 v35, 4, v32
	v_bitop3_b32 v32, v192, v167, 4 bitop3:0x36
	v_cvt_pk_bf16_f32 v75, v14, v15
	s_waitcnt vmcnt(10)
	v_cvt_pk_bf16_f32 v14, v56, v57
	v_lshlrev_b32_e32 v56, 4, v32
	v_bitop3_b32 v32, v192, v167, 8 bitop3:0x36
	v_lshlrev_b32_e32 v57, 4, v32
	v_bitop3_b32 v32, v192, v167, 12 bitop3:0x36
	v_cvt_pk_bf16_f32 v15, v58, v59
	v_lshlrev_b32_e32 v58, 4, v32
	v_lshlrev_b64 v[32:33], 11, v[84:85]
	v_lshl_add_u64 v[178:179], s[0:1], 0, v[32:33]
	v_lshlrev_b64 v[32:33], 11, v[86:87]
	v_lshl_add_u64 v[180:181], s[0:1], 0, v[32:33]
	v_lshlrev_b64 v[32:33], 11, v[88:89]
	v_cvt_pk_bf16_f32 v72, v16, v17
	v_cvt_pk_bf16_f32 v73, v18, v19
	global_store_dwordx4 v[236:237], v[68:71], off
	global_store_dwordx4 v[238:239], v[72:75], off
	global_store_dwordx4 v[240:241], v[76:79], off
	global_store_dwordx4 v[242:243], v[80:83], off
	ds_write_b128 v193, v[68:71]
	ds_write_b128 v193, v[72:75] offset:8192
	ds_write_b128 v193, v[76:79] offset:16384
	ds_write_b128 v193, v[80:83] offset:24576
	v_lshl_add_u32 v34, v167, 8, 0
	v_lshl_add_u64 v[182:183], s[0:1], 0, v[32:33]
	v_lshlrev_b64 v[32:33], 11, v[90:91]
	v_mov_b32_e32 v68, 0
	s_waitcnt vmcnt(13)
	v_cvt_pk_bf16_f32 v16, v60, v61
	v_cvt_pk_bf16_f32 v17, v62, v63
	s_waitcnt vmcnt(12)
	v_cvt_pk_bf16_f32 v18, v64, v65
	v_cvt_pk_bf16_f32 v19, v66, v67
	global_store_dwordx4 v[236:237], v[4:7], off offset:256
	global_store_dwordx4 v[238:239], v[8:11], off offset:256
	global_store_dwordx4 v[240:241], v[12:15], off offset:256
	global_store_dwordx4 v[242:243], v[16:19], off offset:256
	v_lshl_add_u64 v[184:185], s[0:1], 0, v[32:33]
	v_add_u32_e32 v194, v34, v35
	v_add_u32_e32 v195, v34, v56
	v_add_u32_e32 v196, v34, v57
	v_add_u32_e32 v197, v34, v58
	v_mov_b32_e32 v69, v68
	v_mov_b32_e32 v70, v68
	v_mov_b32_e32 v71, v68
	v_mov_b32_e32 v72, v68
	v_mov_b32_e32 v73, v68
	v_mov_b32_e32 v74, v68
	v_mov_b32_e32 v75, v68
	v_mov_b32_e32 v76, v68
	v_mov_b32_e32 v77, v68
	v_mov_b32_e32 v78, v68
	v_mov_b32_e32 v79, v68
	v_mov_b32_e32 v84, v68
	v_mov_b32_e32 v85, v68
	v_mov_b32_e32 v86, v68
	v_mov_b32_e32 v87, v68
	v_mov_b32_e32 v88, v68
	v_mov_b32_e32 v89, v68
	v_mov_b32_e32 v90, v68
	v_mov_b32_e32 v91, v68
	v_mov_b32_e32 v92, v68
	v_mov_b32_e32 v93, v68
	v_mov_b32_e32 v94, v68
	v_mov_b32_e32 v95, v68
	v_mov_b32_e32 v96, v68
	v_mov_b32_e32 v97, v68
	v_mov_b32_e32 v98, v68
	v_mov_b32_e32 v99, v68
	v_mov_b32_e32 v100, v68
	v_mov_b32_e32 v101, v68
	v_mov_b32_e32 v102, v68
	v_mov_b32_e32 v103, v68
	v_mov_b32_e32 v60, v68
	v_mov_b32_e32 v61, v68
	v_mov_b32_e32 v62, v68
	v_mov_b32_e32 v63, v68
	v_mov_b32_e32 v64, v68
	v_mov_b32_e32 v65, v68
	v_mov_b32_e32 v66, v68
	v_mov_b32_e32 v67, v68
	v_mov_b32_e32 v104, v68
	v_mov_b32_e32 v105, v68
	v_mov_b32_e32 v106, v68
	v_mov_b32_e32 v107, v68
	v_mov_b32_e32 v108, v68
	v_mov_b32_e32 v109, v68
	v_mov_b32_e32 v110, v68
	v_mov_b32_e32 v111, v68
	v_mov_b32_e32 v116, v68
	v_mov_b32_e32 v117, v68
	v_mov_b32_e32 v118, v68
	v_mov_b32_e32 v119, v68
	v_mov_b32_e32 v120, v68
	v_mov_b32_e32 v121, v68
	v_mov_b32_e32 v122, v68
	v_mov_b32_e32 v123, v68
	v_mov_b32_e32 v132, v68
	v_mov_b32_e32 v133, v68
	v_mov_b32_e32 v134, v68
	v_mov_b32_e32 v135, v68
	v_mov_b32_e32 v136, v68
	v_mov_b32_e32 v137, v68
	v_mov_b32_e32 v138, v68
	v_mov_b32_e32 v139, v68
	s_waitcnt lgkmcnt(0)
	s_barrier
	s_branch .LBB0_1552

.LBB0_1559:
	v_lshl_add_u64 v[56:57], v[186:187], 1, v[168:169]
	global_load_dwordx4 v[32:35], v[56:57], off

.LBB0_1563:
	v_lshl_add_u64 v[156:157], v[186:187], 1, v[170:171]
	global_load_dwordx4 v[56:59], v[156:157], off

.LBB0_1567:
	v_lshl_add_u64 v[64:65], v[186:187], 1, v[172:173]
	global_load_dwordx4 v[60:63], v[64:65], off

.LBB0_1571:
	v_lshl_add_u64 v[186:187], v[186:187], 1, v[174:175]
	global_load_dwordx4 v[64:67], v[186:187], off

.LBB0_1587:
	v_lshl_add_u64 v[8:9], v[186:187], 1, v[168:169]
	global_load_dwordx4 v[4:7], v[8:9], off

.LBB0_1591:
	v_lshl_add_u64 v[156:157], v[186:187], 1, v[170:171]
	global_load_dwordx4 v[8:11], v[156:157], off

.LBB0_1595:
	v_lshl_add_u64 v[16:17], v[186:187], 1, v[172:173]
	global_load_dwordx4 v[12:15], v[16:17], off

.LBB0_1599:
	v_lshl_add_u64 v[186:187], v[186:187], 1, v[174:175]
	global_load_dwordx4 v[16:19], v[186:187], off

	.amdhsa_kernel _Z6mk_fwd6Params
		.amdhsa_group_segment_fixed_size 0
		.amdhsa_private_segment_fixed_size 0
		.amdhsa_kernarg_size 544
		.amdhsa_user_sgpr_count 2
		.amdhsa_user_sgpr_dispatch_ptr 0
		.amdhsa_user_sgpr_queue_ptr 0
		.amdhsa_user_sgpr_kernarg_segment_ptr 1
		.amdhsa_user_sgpr_dispatch_id 0
		.amdhsa_user_sgpr_kernarg_preload_length 0
		.amdhsa_user_sgpr_kernarg_preload_offset 0
		.amdhsa_user_sgpr_private_segment_size 0
		.amdhsa_uses_dynamic_stack 0
		.amdhsa_enable_private_segment 0
		.amdhsa_system_sgpr_workgroup_id_x 1
		.amdhsa_system_sgpr_workgroup_id_y 0
		.amdhsa_system_sgpr_workgroup_id_z 0
		.amdhsa_system_sgpr_workgroup_info 0
		.amdhsa_system_vgpr_workitem_id 0
		.amdhsa_next_free_vgpr 256
		.amdhsa_next_free_sgpr 100
		.amdhsa_accum_offset 256
		.amdhsa_reserve_vcc 1
		.amdhsa_float_round_mode_32 0
		.amdhsa_float_round_mode_16_64 0
		.amdhsa_float_denorm_mode_32 3
		.amdhsa_float_denorm_mode_16_64 3
		.amdhsa_dx10_clamp 1
		.amdhsa_ieee_mode 1
		.amdhsa_fp16_overflow 0
		.amdhsa_tg_split 0
		.amdhsa_exception_fp_ieee_invalid_op 0
		.amdhsa_exception_fp_denorm_src 0
		.amdhsa_exception_fp_ieee_div_zero 0
		.amdhsa_exception_fp_ieee_overflow 0
		.amdhsa_exception_fp_ieee_underflow 0
		.amdhsa_exception_fp_ieee_inexact 0
		.amdhsa_exception_int_div_zero 0
	.end_amdhsa_kernel

amdhsa.kernels:
  - .agpr_count:     0
    .args:
      - .offset:         0
        .size:           288
        .value_kind:     by_value
      - .offset:         288
        .size:           4
        .value_kind:     hidden_block_count_x
      - .offset:         292
        .size:           4
        .value_kind:     hidden_block_count_y
      - .offset:         296
        .size:           4
        .value_kind:     hidden_block_count_z
      - .offset:         300
        .size:           2
        .value_kind:     hidden_group_size_x
      - .offset:         302
        .size:           2
        .value_kind:     hidden_group_size_y
      - .offset:         304
        .size:           2
        .value_kind:     hidden_group_size_z
      - .offset:         306
        .size:           2
        .value_kind:     hidden_remainder_x
      - .offset:         308
        .size:           2
        .value_kind:     hidden_remainder_y
      - .offset:         310
        .size:           2
        .value_kind:     hidden_remainder_z
      - .offset:         328
        .size:           8
        .value_kind:     hidden_global_offset_x
      - .offset:         336
        .size:           8
        .value_kind:     hidden_global_offset_y
      - .offset:         344
        .size:           8
        .value_kind:     hidden_global_offset_z
      - .offset:         352
        .size:           2
        .value_kind:     hidden_grid_dims
      - .offset:         408
        .size:           4
        .value_kind:     hidden_dynamic_lds_size
    .group_segment_fixed_size: 0
    .kernarg_segment_align: 8
    .kernarg_segment_size: 544
    .language:       OpenCL C
    .language_version:
      - 2
      - 0
    .max_flat_workgroup_size: 512
    .name:           _Z6mk_fwd6Params
    .private_segment_fixed_size: 0
    .sgpr_count:     106
    .sgpr_spill_count: 340
    .symbol:         _Z6mk_fwd6Params.kd
    .uniform_work_group_size: 1
    .uses_dynamic_stack: false
    .vgpr_count:     256
    .vgpr_spill_count: 0
    .wavefront_size: 64
